# baseline (speedup 1.0000x reference)
_Z6gat_k1PKfS0_S0_S0_PDF16_S1_S1_Pf:
	s_load_dwordx8 s[4:11], s[0:1], 0x0
	s_load_dwordx8 s[12:19], s[0:1], 0x20
	v_lshrrev_b32_e32 v54, 6, v0
	v_bfe_u32 v123, v0, 4, 2
	v_and_b32_e32 v120, 15, v0
	v_lshlrev_b32_e32 v120, 4, v120
	v_lshl_or_b32 v120, v54, 8, v120
	v_mov_b32_e32 v121, 0
	v_and_b32_e32 v57, 0xc0, v0
	s_lshl_b32 s3, s2, 5
	v_and_b32_e32 v1, 63, v0
	v_bfe_u32 v55, v0, 5, 1
	v_lshlrev_b32_e32 v2, 8, v57
	v_mov_b32_e32 v19, 0
	v_or_b32_e32 v4, s3, v123
	v_and_b32_e32 v56, 31, v0
	v_lshl_or_b32 v18, v55, 11, v2
	v_lshlrev_b32_e32 v20, 4, v1
	v_mov_b32_e32 v21, v19
	v_ashrrev_i32_e32 v5, 31, v4
	s_waitcnt lgkmcnt(0)
	v_lshl_add_u64 v[2:3], s[6:7], 0, v[18:19]
	v_lshlrev_b32_e32 v18, 2, v56
	s_lshl_b32 s20, s3, 10
	s_add_u32 s20, s4, s20
	s_addc_u32 s21, s5, 0
	v_lshl_or_b32 v121, v123, 10, v120
	global_load_dwordx4 v[22:25], v121, s[20:21] nt
	s_add_u32 s20, s20, 0x1000
	s_addc_u32 s21, s21, 0
	global_load_dwordx4 v[26:29], v121, s[20:21] nt
	s_add_u32 s20, s20, 0x1000
	s_addc_u32 s21, s21, 0
	global_load_dwordx4 v[30:33], v121, s[20:21] nt
	s_add_u32 s20, s20, 0x1000
	s_addc_u32 s21, s21, 0
	global_load_dwordx4 v[34:37], v121, s[20:21] nt
	s_add_u32 s20, s20, 0x1000
	s_addc_u32 s21, s21, 0
	global_load_dwordx4 v[38:41], v121, s[20:21] nt
	s_add_u32 s20, s20, 0x1000
	s_addc_u32 s21, s21, 0
	global_load_dwordx4 v[42:45], v121, s[20:21] nt
	s_add_u32 s20, s20, 0x1000
	s_addc_u32 s21, s21, 0
	global_load_dwordx4 v[46:49], v121, s[20:21] nt
	s_add_u32 s20, s20, 0x1000
	s_addc_u32 s21, s21, 0
	global_load_dwordx4 v[50:53], v121, s[20:21] nt
	s_movk_i32 s4, 0x410
	v_mad_u32_u24 v122, v123, s4, v120
	v_lshl_add_u64 v[2:3], v[2:3], 0, v[18:19]
	v_lshl_add_u64 v[2:3], v[2:3], 0, v[18:19]
	s_movk_i32 s22, 0x1000
	s_mov_b32 s23, 0
	v_lshl_add_u64 v[4:5], v[2:3], 0, s[22:23]
	s_movk_i32 s22, 0x3000
	v_lshl_add_u64 v[6:7], v[2:3], 0, s[22:23]
	global_load_dwordx2 v[58:59], v[4:5], off offset:-4096
	global_load_dwordx2 v[60:61], v[4:5], off offset:-3840
	global_load_dwordx2 v[62:63], v[4:5], off offset:-3584
	global_load_dwordx2 v[64:65], v[4:5], off offset:-3328
	global_load_dwordx2 v[66:67], v[4:5], off offset:-3072
	global_load_dwordx2 v[68:69], v[4:5], off offset:-2816
	global_load_dwordx2 v[70:71], v[4:5], off offset:-2560
	global_load_dwordx2 v[72:73], v[4:5], off offset:-2304
	global_load_dwordx2 v[74:75], v[4:5], off
	global_load_dwordx2 v[76:77], v[4:5], off offset:256
	global_load_dwordx2 v[78:79], v[4:5], off offset:512
	global_load_dwordx2 v[80:81], v[4:5], off offset:768
	global_load_dwordx2 v[82:83], v[4:5], off offset:1024
	global_load_dwordx2 v[84:85], v[4:5], off offset:1280
	global_load_dwordx2 v[86:87], v[4:5], off offset:1536
	global_load_dwordx2 v[88:89], v[4:5], off offset:1792
	global_load_dwordx2 v[90:91], v[6:7], off offset:-4096
	global_load_dwordx2 v[92:93], v[6:7], off offset:-3840
	global_load_dwordx2 v[94:95], v[6:7], off offset:-3584
	global_load_dwordx2 v[96:97], v[6:7], off offset:-3328
	global_load_dwordx2 v[98:99], v[6:7], off offset:-3072
	global_load_dwordx2 v[100:101], v[6:7], off offset:-2816
	global_load_dwordx2 v[102:103], v[6:7], off offset:-2560
	global_load_dwordx2 v[104:105], v[6:7], off offset:-2304
	global_load_dwordx2 v[106:107], v[6:7], off
	global_load_dwordx2 v[108:109], v[6:7], off offset:256
	global_load_dwordx2 v[110:111], v[6:7], off offset:512
	global_load_dwordx2 v[112:113], v[6:7], off offset:768
	global_load_dwordx2 v[114:115], v[6:7], off offset:1024
	global_load_dwordx2 v[116:117], v[6:7], off offset:1280
	global_load_dwordx2 v[118:119], v[6:7], off offset:1536
	global_load_dwordx2 v[120:121], v[6:7], off offset:1792
	v_and_b32_e32 v1, 7, v0
	v_lshlrev_b32_e32 v123, 5, v1
	global_load_dwordx4 v[6:9], v123, s[8:9]
	global_load_dwordx4 v[2:5], v123, s[10:11]
	global_load_dwordx4 v[14:17], v123, s[8:9] offset:16
	global_load_dwordx4 v[10:13], v123, s[10:11] offset:16
	s_movk_i32 s8, 0x110
	s_waitcnt vmcnt(36)
	ds_write_b128 v122, v[22:25] offset:34816
	ds_write_b128 v122, v[26:29] offset:38976
	ds_write_b128 v122, v[30:33] offset:43136
	ds_write_b128 v122, v[34:37] offset:47296
	ds_write_b128 v122, v[38:41] offset:51456
	ds_write_b128 v122, v[42:45] offset:55616
	s_waitcnt vmcnt(36)
	ds_write_b128 v122, v[46:49] offset:59776
	s_waitcnt vmcnt(36)
	ds_write_b128 v122, v[50:53] offset:63936
	v_mul_u32_u24_e32 v22, 0x410, v56
	v_lshlrev_b32_e32 v23, 2, v57
	v_and_b32_e32 v24, 32, v0
	v_add3_u32 v38, v22, v23, v24
	s_waitcnt lgkmcnt(0)
	ds_read_b128 v[22:25], v38 offset:34832
	ds_read_b128 v[26:29], v38 offset:34816
	ds_read_b128 v[30:33], v38 offset:34880
	ds_read_b128 v[34:37], v38 offset:34896
	s_waitcnt lgkmcnt(3)
	v_cvt_pk_f16_f32 v25, v24, v25
	v_cvt_pk_f16_f32 v24, v22, v23
	s_waitcnt lgkmcnt(2)
	v_cvt_pk_f16_f32 v23, v28, v29
	v_cvt_pk_f16_f32 v22, v26, v27
	s_waitcnt vmcnt(28)
	v_cvt_pk_f16_f32 v29, v70, v72
	v_cvt_pk_f16_f32 v28, v66, v68
	v_cvt_pk_f16_f32 v27, v62, v64
	v_cvt_pk_f16_f32 v26, v58, v60
	v_lshlrev_b32_e32 v19, 2, v55
	s_nop 0
	v_mfma_f32_32x32x16_f16 a[0:15], v[22:25], v[26:29], 0
	s_waitcnt vmcnt(28)
	v_cvt_pk_f16_f32 v29, v71, v73
	v_cvt_pk_f16_f32 v28, v67, v69
	v_cvt_pk_f16_f32 v27, v63, v65
	v_cvt_pk_f16_f32 v26, v59, v61
	s_nop 1
	v_mfma_f32_32x32x16_f16 a[16:31], v[22:25], v[26:29], 0
	s_waitcnt lgkmcnt(0)
	v_cvt_pk_f16_f32 v25, v36, v37
	v_cvt_pk_f16_f32 v24, v34, v35
	v_cvt_pk_f16_f32 v23, v32, v33
	v_cvt_pk_f16_f32 v22, v30, v31
	ds_read_b128 v[30:33], v38 offset:34944
	ds_read_b128 v[34:37], v38 offset:34960
	s_waitcnt vmcnt(20)
	v_cvt_pk_f16_f32 v29, v86, v88
	v_cvt_pk_f16_f32 v28, v82, v84
	v_cvt_pk_f16_f32 v27, v78, v80
	s_waitcnt vmcnt(20)
	v_cvt_pk_f16_f32 v26, v74, v76
	s_nop 1
	v_mfma_f32_32x32x16_f16 a[0:15], v[22:25], v[26:29], a[0:15]
	v_cvt_pk_f16_f32 v29, v87, v89
	v_cvt_pk_f16_f32 v28, v83, v85
	v_cvt_pk_f16_f32 v27, v79, v81
	v_cvt_pk_f16_f32 v26, v75, v77
	s_nop 1
	v_mfma_f32_32x32x16_f16 a[16:31], v[22:25], v[26:29], a[16:31]
	s_waitcnt lgkmcnt(0)
	v_cvt_pk_f16_f32 v25, v36, v37
	v_cvt_pk_f16_f32 v24, v34, v35
	v_cvt_pk_f16_f32 v23, v32, v33
	v_cvt_pk_f16_f32 v22, v30, v31
	ds_read_b128 v[30:33], v38 offset:35008
	ds_read_b128 v[34:37], v38 offset:35024
	s_waitcnt vmcnt(12)
	v_cvt_pk_f16_f32 v29, v102, v104
	v_cvt_pk_f16_f32 v28, v98, v100
	v_cvt_pk_f16_f32 v27, v94, v96
	v_cvt_pk_f16_f32 v26, v90, v92
	s_nop 1
	v_mfma_f32_32x32x16_f16 a[0:15], v[22:25], v[26:29], a[0:15]
	s_waitcnt vmcnt(12)
	v_cvt_pk_f16_f32 v29, v103, v105
	v_cvt_pk_f16_f32 v28, v99, v101
	v_cvt_pk_f16_f32 v27, v95, v97
	v_cvt_pk_f16_f32 v26, v91, v93
	s_nop 1
	v_mfma_f32_32x32x16_f16 a[16:31], v[22:25], v[26:29], a[16:31]
	s_waitcnt lgkmcnt(0)
	v_cvt_pk_f16_f32 v25, v36, v37
	v_cvt_pk_f16_f32 v24, v34, v35
	v_cvt_pk_f16_f32 v23, v32, v33
	v_cvt_pk_f16_f32 v22, v30, v31
	s_waitcnt vmcnt(4)
	v_cvt_pk_f16_f32 v29, v118, v120
	v_cvt_pk_f16_f32 v28, v114, v116
	v_cvt_pk_f16_f32 v27, v110, v112
	v_cvt_pk_f16_f32 v26, v106, v108
	s_nop 1
	v_mfma_f32_32x32x16_f16 a[0:15], v[22:25], v[26:29], a[0:15]
	s_waitcnt vmcnt(4)
	v_cvt_pk_f16_f32 v29, v119, v121
	v_cvt_pk_f16_f32 v28, v115, v117
	v_cvt_pk_f16_f32 v27, v111, v113
	v_cvt_pk_f16_f32 v26, v107, v109
	s_nop 1
	v_mfma_f32_32x32x16_f16 a[16:31], v[22:25], v[26:29], a[16:31]
	v_lshl_or_b32 v22, v54, 5, v19
	v_mul_u32_u24_e32 v22, 0x44, v22
	v_lshl_add_u32 v22, v22, 2, v18
	v_add_u32_e32 v22, v22, v18
	v_add_u32_e32 v23, 0x880, v22
	v_add_u32_e32 v24, 0x1100, v22
	v_add_u32_e32 v25, 0x1980, v22
	s_nop 5
	ds_write2_b32 v22, a0, a16 offset1:1
	ds_write2_b32 v22, a1, a17 offset0:68 offset1:69
	ds_write2_b32 v22, a2, a18 offset0:136 offset1:137
	ds_write2_b32 v22, a3, a19 offset0:204 offset1:205
	ds_write2_b32 v23, a4, a20 offset1:1
	ds_write2_b32 v23, a5, a21 offset0:68 offset1:69
	ds_write2_b32 v23, a6, a22 offset0:136 offset1:137
	ds_write2_b32 v23, a7, a23 offset0:204 offset1:205
	ds_write2_b32 v24, a8, a24 offset1:1
	ds_write2_b32 v24, a9, a25 offset0:68 offset1:69
	ds_write2_b32 v24, a10, a26 offset0:136 offset1:137
	ds_write2_b32 v24, a11, a27 offset0:204 offset1:205
	ds_write2_b32 v25, a12, a28 offset1:1
	ds_write2_b32 v25, a13, a29 offset0:68 offset1:69
	ds_write2_b32 v25, a14, a30 offset0:136 offset1:137
	ds_write2_b32 v25, a15, a31 offset0:204 offset1:205
	v_lshrrev_b32_e32 v22, 3, v0
	v_mad_u32_u24 v23, v22, s8, v123
	s_waitcnt lgkmcnt(0)
	s_barrier
	ds_read_b128 v[24:27], v23
	ds_read_b128 v[28:31], v23 offset:16
	ds_read_b128 v[32:35], v23 offset:8704
	s_waitcnt lgkmcnt(2)
	v_pk_add_f32 v[36:37], v[26:27], 0 op_sel_hi:[1,0]
	v_pk_add_f32 v[38:39], v[24:25], 0 op_sel_hi:[1,0]
	ds_read_b128 v[24:27], v23 offset:8720
	s_waitcnt lgkmcnt(2)
	v_pk_add_f32 v[40:41], v[30:31], 0 op_sel_hi:[1,0]
	v_pk_add_f32 v[42:43], v[28:29], 0 op_sel_hi:[1,0]
	ds_read_b128 v[28:31], v23 offset:17408
	s_waitcnt lgkmcnt(2)
	v_pk_add_f32 v[34:35], v[36:37], v[34:35]
	v_pk_add_f32 v[36:37], v[38:39], v[32:33]
	s_waitcnt lgkmcnt(1)
	v_pk_add_f32 v[38:39], v[40:41], v[26:27]
	v_pk_add_f32 v[40:41], v[42:43], v[24:25]
	ds_read_b128 v[24:27], v23 offset:17424
	s_waitcnt lgkmcnt(1)
	v_pk_add_f32 v[42:43], v[34:35], v[30:31]
	ds_read_b128 v[30:33], v23 offset:26112
	v_pk_add_f32 v[28:29], v[36:37], v[28:29]
	ds_read_b128 v[34:37], v23 offset:26128
	s_waitcnt lgkmcnt(2)
	v_pk_add_f32 v[40:41], v[40:41], v[24:25]
	v_pk_add_f32 v[38:39], v[38:39], v[26:27]
	s_waitcnt lgkmcnt(1)
	v_pk_add_f32 v[24:25], v[28:29], v[30:31]
	v_pk_add_f32 v[26:27], v[42:43], v[32:33]
	s_waitcnt lgkmcnt(0)
	v_pk_add_f32 v[28:29], v[40:41], v[34:35]
	v_pk_add_f32 v[30:31], v[38:39], v[36:37]
	s_waitcnt vmcnt(0)
	v_mul_f32_e32 v10, v28, v10
	v_fmac_f32_e32 v10, v24, v2
	v_mul_f32_e32 v14, v28, v14
	v_add_f32_e32 v2, 0, v10
	v_mul_f32_e32 v10, v29, v15
	v_fmac_f32_e32 v14, v24, v6
	v_fmac_f32_e32 v10, v25, v7
	v_mul_f32_e32 v7, v29, v11
	v_add_f32_e32 v6, 0, v14
	v_fmac_f32_e32 v7, v25, v3
	v_mul_f32_e32 v3, v30, v16
	v_add_f32_e32 v6, v6, v10
	v_fmac_f32_e32 v3, v26, v8
	v_add_f32_e32 v3, v6, v3
	v_mul_f32_e32 v6, v30, v12
	v_fmac_f32_e32 v6, v26, v4
	v_mul_f32_e32 v4, v31, v17
	v_fmac_f32_e32 v4, v27, v9
	v_add_f32_e32 v2, v2, v7
	v_add_f32_e32 v3, v3, v4
	v_mul_f32_e32 v4, v31, v13
	v_add_f32_e32 v2, v2, v6
	v_fmac_f32_e32 v4, v27, v5
	v_add_f32_e32 v2, v2, v4
	ds_write_b128 v23, v[24:27]
	ds_write_b128 v23, v[28:31] offset:16
	s_nop 1
	v_add_f32_dpp v3, v3, v3 quad_perm:[1,0,3,2] row_mask:0xf bank_mask:0xf
	v_add_f32_dpp v6, v2, v2 quad_perm:[1,0,3,2] row_mask:0xf bank_mask:0xf
	s_nop 1
	v_add_f32_dpp v3, v3, v3 quad_perm:[2,3,0,1] row_mask:0xf bank_mask:0xf
	v_add_f32_dpp v6, v6, v6 quad_perm:[2,3,0,1] row_mask:0xf bank_mask:0xf
	s_nop 1
	v_add_f32_dpp v2, v3, v3 row_half_mirror row_mask:0xf bank_mask:0xf
	v_add_f32_dpp v3, v6, v6 row_half_mirror row_mask:0xf bank_mask:0xf
	v_cmp_eq_u32_e32 vcc, 0, v1
	s_and_saveexec_b64 s[6:7], vcc
	s_cbranch_execz .LBB0_2
	v_mul_f32_e32 v4, 0x3f7d70a4, v3
	v_mul_f32_e32 v4, 0x3fb8aa3b, v4
	v_mul_f32_e32 v3, 0x3c23d70a, v3
	v_exp_f32_e32 v4, v4
	v_mul_f32_e32 v3, 0x3fb8aa3b, v3
	v_exp_f32_e32 v3, v3
	v_lshlrev_b32_e32 v5, 2, v22
	v_or_b32_e32 v6, 0x10a80, v5
	v_mul_f32_e32 v2, 0xbf7d70a4, v2
	ds_write_b32 v6, v4
	v_or_b32_e32 v4, 0x10a00, v5
	v_mul_f32_e32 v2, 0x3fb8aa3b, v2
	ds_write_b32 v4, v3
	v_exp_f32_e32 v4, v2
	v_add_u32_e32 v2, s3, v22
	v_ashrrev_i32_e32 v3, 31, v2
	v_lshl_add_u64 v[2:3], v[2:3], 2, s[18:19]
	global_store_dword v[2:3], v4, off sc0 sc1
.LBB0_2:
	s_or_b64 exec, exec, s[6:7]
	v_bfe_u32 v16, v0, 6, 1
	v_lshl_or_b32 v2, v16, 4, v19
	s_movk_i32 s6, 0x80
	v_and_or_b32 v3, v0, s6, v18
	v_lshlrev_b32_e32 v6, 2, v2
	v_mad_u32_u24 v12, v2, s8, v3
	v_or_b32_e32 v2, 0x10a00, v6
	v_or_b32_e32 v6, 0x10a20, v6
	v_add_u32_e32 v14, 0x800, v12
	v_lshlrev_b32_e32 v50, 2, v0
	v_and_b32_e32 v50, 0x200, v50
	v_lshl_add_u32 v50, s2, 1, v50
	v_or_b32_e32 v50, v50, v16
	v_ashrrev_i32_e32 v51, 31, v50
	v_lshlrev_b64 v[50:51], 10, v[50:51]
	v_lshl_add_u64 v[50:51], s[12:13], 0, v[50:51]
	v_lshl_add_u64 v[50:51], v[50:51], 0, v[20:21]
	v_lshlrev_b32_e32 v40, 1, v0
	v_bfe_u32 v41, v0, 3, 1
	v_and_b32_e32 v40, 8, v40
	v_and_b32_e32 v42, 16, v0
	v_and_or_b32 v43, v0, 3, v40
	v_lshlrev_b32_e32 v40, 2, v41
	v_or3_b32 v43, v43, v40, v42
	v_lshlrev_b32_e32 v43, 2, v43
	v_or_b32_e32 v44, 0x10a80, v43
	v_or_b32_e32 v45, 0x10a00, v43
	v_lshl_or_b32 v46, v41, 3, s3
	v_or3_b32 v46, v46, v42, v1
	v_ashrrev_i32_e32 v47, 31, v46
	v_lshlrev_b64 v[46:47], 1, v[46:47]
	v_lshl_add_u64 v[48:49], s[14:15], 0, v[46:47]
	v_lshl_add_u64 v[46:47], s[16:17], 0, v[46:47]
	v_cmp_gt_u32_e32 vcc, 32, v0
	s_waitcnt lgkmcnt(0)
	s_barrier
	ds_read2_b32 v[10:11], v12 offset1:68
	ds_read_b128 v[2:5], v2
	ds_read_b128 v[6:9], v6
	ds_read2_b32 v[52:53], v12 offset0:136 offset1:204
	ds_read2_b32 v[12:13], v14 offset0:32 offset1:100
	ds_read2_b32 v[14:15], v14 offset0:168 offset1:236
	ds_read_b32 v44, v44
	ds_read_b32 v45, v45
	s_waitcnt lgkmcnt(6)
	v_pk_mul_f32 v[2:3], v[10:11], v[2:3]
	s_waitcnt lgkmcnt(4)
	v_pk_mul_f32 v[4:5], v[52:53], v[4:5]
	v_cvt_pk_f16_f32 v2, v2, v3
	v_cvt_pk_f16_f32 v3, v4, v5
	s_waitcnt lgkmcnt(3)
	v_pk_mul_f32 v[4:5], v[12:13], v[6:7]
	s_waitcnt lgkmcnt(2)
	v_pk_mul_f32 v[6:7], v[14:15], v[8:9]
	v_cvt_pk_f16_f32 v4, v4, v5
	v_cvt_pk_f16_f32 v5, v6, v7
	global_store_dwordx4 v[50:51], v[2:5], off sc0 sc1
	s_and_saveexec_b64 s[4:5], vcc
	s_cbranch_execz .LBB0_4
	s_waitcnt lgkmcnt(0)
	v_cvt_f16_f32_e32 v44, v44
	v_cvt_f16_f32_e32 v45, v45
	global_store_short v[48:49], v44, off sc0 sc1
	global_store_short v[46:47], v45, off sc0 sc1
